# adds top-k bisection: 4 of 8 per-lane carry adds per block moved to scalar popcounts
# speedup vs baseline: 1.0086x; 1.0029x over previous
.LBB0_416:
	s_nop 0
	v_add_u32_dpp v133, v133, v133 row_ror:8 row_mask:0xf bank_mask:0xf bound_ctrl:1
	s_nop 1
	v_add_u32_dpp v133, v133, v133 row_ror:4 row_mask:0xf bank_mask:0xf bound_ctrl:1
	s_nop 1
	v_add_u32_dpp v133, v133, v133 row_ror:2 row_mask:0xf bank_mask:0xf bound_ctrl:1
	s_nop 1
	v_add_u32_dpp v133, v133, v133 row_ror:1 row_mask:0xf bank_mask:0xf bound_ctrl:1
	s_nop 0
	v_readlane_b32 s80, v133, 0
	v_readlane_b32 s81, v133, 16
	s_add_i32 s80, s81, s80
	v_readlane_b32 s81, v133, 32
	s_add_i32 s80, s80, s81
	v_readlane_b32 s81, v133, 48
	s_add_i32 s82, s80, s81
	s_add_i32 s82, s82, s98
	s_cmpk_lg_i32 s82, 0x100
	s_cselect_b64 s[80:81], -1, 0
	s_cmpk_lt_i32 s82, 0x100
	s_cselect_b64 vcc, -1, 0
	v_cndmask_b32_e32 v71, v131, v71, vcc
	v_add_co_u32_e32 v123, vcc, -1, v123
	s_cselect_b32 s14, s14, s82
	s_and_b64 s[80:81], s[80:81], vcc
	s_and_b64 vcc, exec, s[80:81]
	s_cbranch_vccz .LBB0_425
.LBB0_417:
	v_lshlrev_b32_e64 v131, v123, 1
	v_or_b32_e32 v131, v71, v131
	v_mov_b32_e32 v133, 0
	s_mov_b32 s98, 0
	s_andn2_b64 vcc, exec, s[44:45]
	v_cmp_ge_u32_e64 s[80:81], v111, v131
	v_cmp_ge_u32_e64 s[82:83], v130, v131
	v_cmp_ge_u32_e64 s[84:85], v109, v131
	v_cmp_ge_u32_e64 s[86:87], v1, v131
	v_cmp_ge_u32_e64 s[88:89], v2, v131
	v_cmp_ge_u32_e64 s[90:91], v129, v131
	v_cmp_ge_u32_e64 s[92:93], v128, v131
	v_cmp_ge_u32_e64 s[94:95], v127, v131
	v_addc_co_u32_e64 v133, s[96:97], 0, v133, s[80:81]
	v_addc_co_u32_e64 v133, s[96:97], 0, v133, s[82:83]
	v_addc_co_u32_e64 v133, s[96:97], 0, v133, s[84:85]
	v_addc_co_u32_e64 v133, s[96:97], 0, v133, s[86:87]
	s_bcnt1_i32_b64 s99, s[88:89]
	s_add_i32 s98, s98, s99
	s_bcnt1_i32_b64 s99, s[90:91]
	s_add_i32 s98, s98, s99
	s_bcnt1_i32_b64 s99, s[92:93]
	s_add_i32 s98, s98, s99
	s_bcnt1_i32_b64 s99, s[94:95]
	s_add_i32 s98, s98, s99
	s_cbranch_vccnz .LBB0_421
	v_cmp_ge_u32_e64 s[80:81], v4, v131
	v_cmp_ge_u32_e64 s[82:83], v126, v131
	v_cmp_ge_u32_e64 s[84:85], v125, v131
	v_cmp_ge_u32_e64 s[86:87], v124, v131
	v_cmp_ge_u32_e64 s[88:89], v122, v131
	v_cmp_ge_u32_e64 s[90:91], v121, v131
	v_cmp_ge_u32_e64 s[92:93], v120, v131
	v_cmp_ge_u32_e64 s[94:95], v119, v131
	v_addc_co_u32_e64 v133, s[96:97], 0, v133, s[80:81]
	v_addc_co_u32_e64 v133, s[96:97], 0, v133, s[82:83]
	v_addc_co_u32_e64 v133, s[96:97], 0, v133, s[84:85]
	v_addc_co_u32_e64 v133, s[96:97], 0, v133, s[86:87]
	s_bcnt1_i32_b64 s99, s[88:89]
	s_add_i32 s98, s98, s99
	s_bcnt1_i32_b64 s99, s[90:91]
	s_add_i32 s98, s98, s99
	s_bcnt1_i32_b64 s99, s[92:93]
	s_add_i32 s98, s98, s99
	s_bcnt1_i32_b64 s99, s[94:95]
	s_add_i32 s98, s98, s99
	s_andn2_b64 vcc, exec, s[60:61]
	s_cbranch_vccz .LBB0_422

.LBB0_420:
	v_cmp_ge_u32_e64 s[80:81], v102, v131
	v_cmp_ge_u32_e64 s[82:83], v100, v131
	v_cmp_ge_u32_e64 s[84:85], v99, v131
	v_cmp_ge_u32_e64 s[86:87], v98, v131
	v_cmp_ge_u32_e64 s[88:89], v97, v131
	v_cmp_ge_u32_e64 s[90:91], v96, v131
	v_cmp_ge_u32_e64 s[92:93], v95, v131
	v_cmp_ge_u32_e64 s[94:95], v94, v131
	v_addc_co_u32_e64 v133, s[96:97], 0, v133, s[80:81]
	v_addc_co_u32_e64 v133, s[96:97], 0, v133, s[82:83]
	v_addc_co_u32_e64 v133, s[96:97], 0, v133, s[84:85]
	v_addc_co_u32_e64 v133, s[96:97], 0, v133, s[86:87]
	s_bcnt1_i32_b64 s99, s[88:89]
	s_add_i32 s98, s98, s99
	s_bcnt1_i32_b64 s99, s[90:91]
	s_add_i32 s98, s98, s99
	s_bcnt1_i32_b64 s99, s[92:93]
	s_add_i32 s98, s98, s99
	s_bcnt1_i32_b64 s99, s[94:95]
	s_add_i32 s98, s98, s99
	s_nop 0
	v_cmp_ge_u32_e64 s[80:81], v93, v131
	v_cmp_ge_u32_e64 s[82:83], v92, v131
	v_cmp_ge_u32_e64 s[84:85], v91, v131
	v_cmp_ge_u32_e64 s[86:87], v90, v131
	v_cmp_ge_u32_e64 s[88:89], v89, v131
	v_cmp_ge_u32_e64 s[90:91], v88, v131
	v_cmp_ge_u32_e64 s[92:93], v87, v131
	v_cmp_ge_u32_e64 s[94:95], v86, v131
	v_addc_co_u32_e64 v133, s[96:97], 0, v133, s[80:81]
	v_addc_co_u32_e64 v133, s[96:97], 0, v133, s[82:83]
	v_addc_co_u32_e64 v133, s[96:97], 0, v133, s[84:85]
	v_addc_co_u32_e64 v133, s[96:97], 0, v133, s[86:87]
	s_bcnt1_i32_b64 s99, s[88:89]
	s_add_i32 s98, s98, s99
	s_bcnt1_i32_b64 s99, s[90:91]
	s_add_i32 s98, s98, s99
	s_bcnt1_i32_b64 s99, s[92:93]
	s_add_i32 s98, s98, s99
	s_bcnt1_i32_b64 s99, s[94:95]
	s_add_i32 s98, s98, s99
	s_andn2_b64 vcc, exec, s[48:49]
	s_cbranch_vccnz .LBB0_416
	s_branch .LBB0_424

.LBB0_422:
	v_cmp_ge_u32_e64 s[80:81], v5, v131
	v_cmp_ge_u32_e64 s[82:83], v118, v131
	v_cmp_ge_u32_e64 s[84:85], v117, v131
	v_cmp_ge_u32_e64 s[86:87], v116, v131
	v_cmp_ge_u32_e64 s[88:89], v115, v131
	v_cmp_ge_u32_e64 s[90:91], v114, v131
	v_cmp_ge_u32_e64 s[92:93], v113, v131
	v_cmp_ge_u32_e64 s[94:95], v112, v131
	v_addc_co_u32_e64 v133, s[96:97], 0, v133, s[80:81]
	v_addc_co_u32_e64 v133, s[96:97], 0, v133, s[82:83]
	v_addc_co_u32_e64 v133, s[96:97], 0, v133, s[84:85]
	v_addc_co_u32_e64 v133, s[96:97], 0, v133, s[86:87]
	s_bcnt1_i32_b64 s99, s[88:89]
	s_add_i32 s98, s98, s99
	s_bcnt1_i32_b64 s99, s[90:91]
	s_add_i32 s98, s98, s99
	s_bcnt1_i32_b64 s99, s[92:93]
	s_add_i32 s98, s98, s99
	s_bcnt1_i32_b64 s99, s[94:95]
	s_add_i32 s98, s98, s99
	s_nop 0
	v_cmp_ge_u32_e64 s[80:81], v110, v131
	v_cmp_ge_u32_e64 s[82:83], v108, v131
	v_cmp_ge_u32_e64 s[84:85], v107, v131
	v_cmp_ge_u32_e64 s[86:87], v106, v131
	v_cmp_ge_u32_e64 s[88:89], v105, v131
	v_cmp_ge_u32_e64 s[90:91], v104, v131
	v_cmp_ge_u32_e64 s[92:93], v103, v131
	v_cmp_ge_u32_e64 s[94:95], v101, v131
	v_addc_co_u32_e64 v133, s[96:97], 0, v133, s[80:81]
	v_addc_co_u32_e64 v133, s[96:97], 0, v133, s[82:83]
	v_addc_co_u32_e64 v133, s[96:97], 0, v133, s[84:85]
	v_addc_co_u32_e64 v133, s[96:97], 0, v133, s[86:87]
	s_bcnt1_i32_b64 s99, s[88:89]
	s_add_i32 s98, s98, s99
	s_bcnt1_i32_b64 s99, s[90:91]
	s_add_i32 s98, s98, s99
	s_bcnt1_i32_b64 s99, s[92:93]
	s_add_i32 s98, s98, s99
	s_bcnt1_i32_b64 s99, s[94:95]
	s_add_i32 s98, s98, s99
	s_andn2_b64 vcc, exec, s[12:13]
	s_cbranch_vccz .LBB0_420

.LBB0_424:
	v_cmp_ge_u32_e64 s[80:81], v132, v131
	v_cmp_ge_u32_e64 s[82:83], v85, v131
	v_cmp_ge_u32_e64 s[84:85], v84, v131
	v_cmp_ge_u32_e64 s[86:87], v83, v131
	v_cmp_ge_u32_e64 s[88:89], v82, v131
	v_cmp_ge_u32_e64 s[90:91], v81, v131
	v_cmp_ge_u32_e64 s[92:93], v80, v131
	v_cmp_ge_u32_e64 s[94:95], v79, v131
	v_addc_co_u32_e64 v133, s[96:97], 0, v133, s[80:81]
	v_addc_co_u32_e64 v133, s[96:97], 0, v133, s[82:83]
	v_addc_co_u32_e64 v133, s[96:97], 0, v133, s[84:85]
	v_addc_co_u32_e64 v133, s[96:97], 0, v133, s[86:87]
	s_bcnt1_i32_b64 s99, s[88:89]
	s_add_i32 s98, s98, s99
	s_bcnt1_i32_b64 s99, s[90:91]
	s_add_i32 s98, s98, s99
	s_bcnt1_i32_b64 s99, s[92:93]
	s_add_i32 s98, s98, s99
	s_bcnt1_i32_b64 s99, s[94:95]
	s_add_i32 s98, s98, s99
	s_nop 0
	v_cmp_ge_u32_e64 s[80:81], v78, v131
	v_cmp_ge_u32_e64 s[82:83], v77, v131
	v_cmp_ge_u32_e64 s[84:85], v76, v131
	v_cmp_ge_u32_e64 s[86:87], v75, v131
	v_cmp_ge_u32_e64 s[88:89], v74, v131
	v_cmp_ge_u32_e64 s[90:91], v73, v131
	v_cmp_ge_u32_e64 s[92:93], v72, v131
	v_cmp_ge_u32_e64 s[94:95], v70, v131
	v_addc_co_u32_e64 v133, s[96:97], 0, v133, s[80:81]
	v_addc_co_u32_e64 v133, s[96:97], 0, v133, s[82:83]
	v_addc_co_u32_e64 v133, s[96:97], 0, v133, s[84:85]
	v_addc_co_u32_e64 v133, s[96:97], 0, v133, s[86:87]
	s_bcnt1_i32_b64 s99, s[88:89]
	s_add_i32 s98, s98, s99
	s_bcnt1_i32_b64 s99, s[90:91]
	s_add_i32 s98, s98, s99
	s_bcnt1_i32_b64 s99, s[92:93]
	s_add_i32 s98, s98, s99
	s_bcnt1_i32_b64 s99, s[94:95]
	s_add_i32 s98, s98, s99
	s_branch .LBB0_416
